# full stack + one static s_setprio 1 for waves 4-7 at the attention entry (both layers), reset at the next grid barrier
# baseline (speedup 1.0000x reference)
.LBB0_942:
	s_cmpk_gt_i32 s56, 0x40f
	s_barrier
	s_cbranch_scc1 .LBB0_1085
	v_readfirstlane_b32 s32, v0
	s_nop 3
	s_bfe_u32 s32, s32, 0x40006
	s_cmp_ge_u32 s32, 4
	s_cbranch_scc0 .Laprio_L0
	s_setprio 1
.Laprio_L0:
	s_add_u32 s0, s58, 0x47240000
	v_writelane_b32 v251, s0, 22
	s_addc_u32 s0, s59, 0
	v_writelane_b32 v251, s0, 24
	s_add_u32 s0, s58, 0x4a300000
	v_writelane_b32 v251, s0, 26
	s_addc_u32 s0, s59, 0
	v_writelane_b32 v251, s0, 28
	s_add_u32 s0, s58, 0x4a300800
	v_writelane_b32 v251, s0, 34
	s_addc_u32 s0, s59, 0
	v_writelane_b32 v251, s0, 44
	s_add_u32 s0, s58, 0x47240200
	v_writelane_b32 v251, s0, 30
	s_addc_u32 s0, s59, 0
	v_writelane_b32 v251, s0, 32
	s_movk_i32 s0, 0x1e0
	v_cmp_gt_i32_e64 s[0:1], s0, v182
	v_and_b32_e32 v184, 31, v182
	v_cmp_ne_u32_e64 s[34:35], 31, v184
	v_writelane_b32 v251, s0, 54
	v_lshl_add_u32 v1, v182, 2, 0
	s_mov_b32 s75, 0
	v_writelane_b32 v251, s1, 55
	v_writelane_b32 v251, s34, 48
	v_add_u32_e32 v1, 0x10800, v1
	v_mov_b32_e32 v3, 0
	s_movk_i32 s33, 0x7fff
	v_mov_b32_e32 v183, 0xf9
	v_bfrev_b32_e32 v185, 0.5
	v_mov_b32_e32 v188, 0xf149f2ca
	v_writelane_b32 v251, s35, 49
	s_branch .LBB0_945

.LBB0_2986:
	v_readlane_b32 s0, v254, 4
	v_readlane_b32 s1, v254, 5
	s_and_b64 vcc, exec, s[0:1]
	s_barrier
	s_cbranch_vccz .LBB0_3117
	v_readfirstlane_b32 s32, v0
	s_nop 3
	s_bfe_u32 s32, s32, 0x40006
	s_cmp_ge_u32 s32, 4
	s_cbranch_scc0 .Laprio_L1
	s_setprio 1
.Laprio_L1:
	v_readlane_b32 s36, v254, 0
	v_readlane_b32 s37, v254, 1
	s_add_u32 s16, s36, 0x47240000
	s_addc_u32 s0, s37, 0
	v_writelane_b32 v251, s0, 46
	s_add_u32 s0, s36, 0x4a300000
	v_writelane_b32 v251, s0, 48
	s_addc_u32 s0, s37, 0
	v_writelane_b32 v251, s0, 22
	v_readlane_b32 s0, v250, 44
	v_readlane_b32 s14, v250, 58
	v_readlane_b32 s15, v250, 59
	s_add_u32 s38, s14, 0x3a20
	s_addc_u32 s39, s15, 0
	s_add_u32 s0, s36, 0x4a300800
	v_writelane_b32 v251, s0, 24
	s_addc_u32 s0, s37, 0
	v_writelane_b32 v251, s0, 26
	s_add_u32 s0, s36, 0x47240200
	v_writelane_b32 v251, s0, 28
	s_addc_u32 s0, s37, 0
	v_readlane_b32 s1, v250, 45
	v_writelane_b32 v251, s0, 14
	s_movk_i32 s0, 0x1e0
	v_cmp_gt_i32_e64 s[0:1], s0, v1
	v_readlane_b32 s2, v250, 46
	v_readlane_b32 s3, v250, 47
	v_writelane_b32 v251, s0, 44
	v_readlane_b32 s13, v250, 57
	v_and_b32_e32 v182, 31, v1
	v_writelane_b32 v251, s1, 45
	v_lshl_add_u32 v2, v1, 2, 0
	v_readlane_b32 s34, v251, 38
	v_readlane_b32 s35, v251, 39
	v_writelane_b32 v251, s38, 40
	s_mov_b32 s13, s16
	v_cmp_ne_u32_e64 s[2:3], 31, v182
	s_mov_b32 s79, 0
	v_add_u32_e32 v183, 0x10800, v2
	v_mov_b32_e32 v3, 0
	s_movk_i32 s33, 0x7fff
	v_mov_b32_e32 v186, 0xf9
	v_bfrev_b32_e32 v187, 0.5
	v_mov_b32_e32 v188, 0xf149f2ca
	v_writelane_b32 v251, s39, 41
	v_readlane_b32 s4, v250, 48
	v_readlane_b32 s5, v250, 49
	v_readlane_b32 s6, v250, 50
	v_readlane_b32 s7, v250, 51
	v_readlane_b32 s8, v250, 52
	v_readlane_b32 s9, v250, 53
	v_readlane_b32 s10, v250, 54
	v_readlane_b32 s11, v250, 55
	v_readlane_b32 s12, v250, 56
	s_branch .LBB0_2989
